# attention tile loops (MoBA, forgetting attention): the K/V ring refill is issued at the end of a step, before the wait + barrier opening the next, instead of right after the barrier in front of the fr
# baseline (speedup 1.0000x reference)
; #define LAS __attribute__((address_space(3)))
; __device__ __forceinline__ float bf_lo(unsigned u) { return __uint_as_float(u << 16); }
; __device__ __forceinline__ float bf_hi(unsigned u) { return __uint_as_float(u & 0xffff0000u); }
; __device__ __forceinline__ void attn_fox_unit(Frame& F, const bf16_t* Qh, const bf16_t* Kh, const bf16_t* Vth, const float* CFh, const int qb, bf16_t* AOp, const float k2max) {
;     ...
;     const f32x4 cv = *(const f32x4*)(CFh + 4 * F.tid);
;     { float q2 = 0.f;
; #pragma unroll
;       for (int d0 = 0; d0 < 4; ++d0) { const u32x4 w = __builtin_bit_cast(u32x4, qr[d0]); q2 += (bf_lo(w.x) * bf_lo(w.x) + bf_hi(w.x) * bf_hi(w.x)) + (bf_lo(w.y) * bf_lo(w.y) + bf_hi(w.y) * bf_hi(w.y)) + (bf_lo(w.z) * bf_lo(w.z) + bf_hi(w.z) * bf_hi(w.z)) + (bf_lo(w.w) * bf_lo(w.w) + bf_hi(w.w) * bf_hi(w.w)); }
;       q2 += __shfl_xor(q2, 32); q2 = wave_max(q2); if (lane == 0) xs[wave] = q2; }
;     *(LAS f32x4*)(ring + AT_CF + 16 * F.tid) = -cv;
;     asm volatile("s_waitcnt vmcnt(0) lgkmcnt(0)" ::: "memory"); __builtin_amdgcn_s_barrier();
;     int Tmin;
;     { float q2m = xs[0];
; #pragma unroll
;       for (int k = 1; k < NWAVES; ++k) q2m = fmaxf(q2m, xs[k]);
;       const float B = __builtin_sqrtf(q2m * k2max) * 1.02f + 1.f, cq0 = -*(LAS const float*)(ring + AT_CF + 4 * (256 * qb)), thr = cq0 + 2.f * B + 160.f;
;       const float cnt = wave_total((float)((cv[0] > thr) + (cv[1] > thr) + (cv[2] > thr) + (cv[3] > thr)));
;       if (lane == 0) xs[16 + wave] = cnt;
;       asm volatile("s_waitcnt lgkmcnt(0)" ::: "memory"); __builtin_amdgcn_s_barrier();
;       float tot = xs[16];
; #pragma unroll
;       for (int k = 1; k < NWAVES; ++k) tot += xs[16 + k];
;       Tmin = (int)tot >> 6; if (Tmin > 4 * qb) Tmin = 4 * qb; Tmin = __builtin_amdgcn_readfirstlane(Tmin); }
;     const int NT = 4 * qb + 4, my_last = 4 * qb + (wave >> 1), jdiag = wave & 1;
.LBB0_536:
	s_or_b64 exec, exec, s[0:1]
	s_add_i32 s13, 0, 0x10000
	s_waitcnt vmcnt(0)
	v_xor_b32_e32 v11, 0x80000000, v3
	v_xor_b32_e32 v10, 0x80000000, v2
	s_waitcnt lgkmcnt(0)
	v_xor_b32_e32 v9, 0x80000000, v1
	v_xor_b32_e32 v8, 0x80000000, v0
	v_add_u32_e32 v12, s13, v112
	s_add_i32 s0, 0, 0x12000
	ds_write_b128 v12, v[8:11]
	v_mov_b32_e32 v8, s0
	s_waitcnt vmcnt(0) lgkmcnt(0)
	s_barrier
	ds_read_b128 v[8:11], v8
	s_mov_b32 s0, 0xf800000
	s_lshl_b32 s15, s5, 10
	s_waitcnt lgkmcnt(0)
	v_max_f32_e32 v9, v9, v9
	v_max_f32_e32 v8, v8, v8
	v_max_f32_e32 v8, v8, v9
	v_max3_f32 v12, v8, v10, v11
	v_mov_b32_e32 v8, s90
	ds_read_b128 v[8:11], v8
	s_waitcnt lgkmcnt(0)
	v_max3_f32 v8, v12, v8, v9
	v_max3_f32 v8, v8, v10, v11
	v_mul_f32_e32 v8, v147, v8
	v_cmp_gt_f32_e64 s[0:1], s0, v8
	v_mul_f32_e32 v9, 0x4f800000, v8
	s_nop 0
	v_cndmask_b32_e64 v8, v8, v9, s[0:1]
	v_sqrt_f32_e32 v9, v8
	s_nop 0
	v_add_u32_e32 v10, -1, v9
	v_fma_f32 v11, -v10, v9, v8
	v_cmp_ge_f32_e64 s[20:21], 0, v11
	v_add_u32_e32 v11, 1, v9
	s_nop 0
	v_cndmask_b32_e64 v10, v9, v10, s[20:21]
	v_fma_f32 v9, -v11, v9, v8
	v_cmp_lt_f32_e64 s[20:21], 0, v9
	s_nop 1
	v_cndmask_b32_e64 v9, v10, v11, s[20:21]
	v_mul_f32_e32 v10, 0x37800000, v9
	v_cndmask_b32_e64 v9, v9, v10, s[0:1]
	v_cmp_class_f32_e64 s[0:1], v8, v139
	s_nop 1
	v_cndmask_b32_e64 v8, v9, v8, s[0:1]
	s_mov_b32 s0, 0x3f828f5c
	v_fma_f32 v8, v8, s0, 1.0
	s_add_i32 s0, s13, s15
	v_mov_b32_e32 v9, s0
	ds_read_b32 v9, v9
	s_waitcnt lgkmcnt(0)
	v_fma_f32 v8, v8, 2.0, -v9
	v_add_f32_e32 v8, 0x43200000, v8
	v_cmp_gt_f32_e64 s[20:21], v1, v8
	v_cmp_gt_f32_e64 s[0:1], v0, v8
	s_nop 0
	v_cndmask_b32_e64 v0, 0, 1, s[20:21]
	v_addc_co_u32_e64 v0, s[0:1], 0, v0, s[0:1]
	v_cmp_gt_f32_e64 s[0:1], v2, v8
	s_nop 1
	v_cndmask_b32_e64 v1, 0, 1, s[0:1]
	v_cmp_gt_f32_e64 s[0:1], v3, v8
	s_nop 1
	v_addc_co_u32_e64 v0, s[0:1], v0, v1, s[0:1]
	v_cvt_f32_ubyte0_e32 v0, v0
	v_mov_b32_e32 v1, v115
	s_nop 0
	v_add_f32_dpp v0, v0, v0 row_shr:1 row_mask:0xf bank_mask:0xf bound_ctrl:1
	s_nop 1
	v_add_f32_dpp v0, v0, v0 row_shr:2 row_mask:0xf bank_mask:0xf bound_ctrl:1
	s_nop 1
	v_add_f32_dpp v0, v0, v0 row_shr:4 row_mask:0xf bank_mask:0xf bound_ctrl:1
	s_nop 1
	v_add_f32_dpp v0, v0, v0 row_shr:8 row_mask:0xf bank_mask:0xf bound_ctrl:1
	s_nop 1
	v_mov_b32_dpp v1, v0 row_bcast:15 row_mask:0xa bank_mask:0xf
	v_add_f32_e32 v0, v0, v1
	v_mov_b32_e32 v1, v115
	s_nop 1
	v_mov_b32_dpp v1, v0 row_bcast:31 row_mask:0xc bank_mask:0xf
	v_add_f32_e32 v0, v0, v1
	s_nop 0
	v_readlane_b32 s14, v0, 63
	s_and_saveexec_b64 s[0:1], vcc
	v_mov_b32_e32 v0, s89
	v_mov_b32_e32 v1, s14
	ds_write_b32 v0, v1 offset:64
	s_or_b64 exec, exec, s[0:1]
	s_lshl_b32 s95, s5, 2
	v_lshlrev_b32_e32 v0, 1, v7
	v_lshrrev_b32_e32 v1, 1, v6
	s_or_b32 s1, s95, 3
	v_and_b32_e32 v8, 19, v6
	v_and_b32_e32 v9, 4, v1
	v_and_b32_e32 v10, 8, v0
	s_lshl_b32 s0, s1, 6
	v_or3_b32 v11, v9, v8, v10
	s_add_i32 s0, s0, s17
	v_or_b32_e32 v0, s0, v11
	v_mov_b32_e32 v1, v115
	v_lshlrev_b64 v[0:1], 7, v[0:1]
	v_lshl_add_u64 v[2:3], s[10:11], 0, v[0:1]
	v_lshlrev_b64 v[0:1], 1, v[4:5]
	v_lshl_add_u64 v[12:13], v[2:3], 0, v[0:1]
	v_lshl_or_b32 v2, v7, 12, s31
	v_mov_b32_e32 v3, v115
	v_lshl_add_u64 v[2:3], s[6:7], 0, v[2:3]
	s_lshl_b32 s92, s1, 7
	v_lshl_add_u64 v[14:15], v[2:3], 0, s[92:93]
	s_lshl_b32 s92, s17, 1
	v_lshl_add_u64 v[14:15], v[14:15], 0, s[92:93]
	s_mov_b32 s5, s93
	s_add_i32 s14, s18, 0
	s_add_i32 s0, s17, s12
	v_lshl_add_u64 v[14:15], v[14:15], 0, s[4:5]
	s_mov_b32 m0, s14
	s_add_i32 s22, s19, 0
	s_add_i32 s20, s0, 0x80
	s_waitcnt lgkmcnt(0)
	s_barrier
; __device__ __forceinline__ void attn_fox_unit(Frame& F, const bf16_t* Qh, const bf16_t* Kh, const bf16_t* Vth, const float* CFh, const int qb, bf16_t* AOp, const float k2max) {
;     ...
;       Tmin = (int)tot >> 6; if (Tmin > 4 * qb) Tmin = 4 * qb; Tmin = __builtin_amdgcn_readfirstlane(Tmin); }
;     const int NT = 4 * qb + 4, my_last = 4 * qb + (wave >> 1), jdiag = wave & 1;
;     attn_dma_tile(Kh, Vth, NT - 1, ring, wave, r32, r32p, hi);
;     attn_dma_tile(Kh, Vth, NT - 2, ring + AT_SLOT, wave, r32, r32p, hi);
;     attn_dma_tile(Kh, Vth, NT - 3, ring + 2 * AT_SLOT, wave, r32, r32p, hi);
;     f32x16 O0 = f32x16{}, O1 = f32x16{}; float m = -INFINITY, l = 0.f;
;     int slot = 0;
; #pragma unroll 1
;     for (int T = NT - 1; T >= Tmin; --T) {
	v_lshl_add_u64 v[14:15], v[14:15], 0, v[0:1]
	global_load_lds_dwordx4 v[12:13], off
	s_add_i32 m0, s22, 0x2000
	v_or_b32_e32 v12, s20, v11
	s_lshl_b32 s20, s12, 1
	s_mov_b32 s21, s93
	global_load_lds_dwordx4 v[14:15], off
	v_lshl_add_u64 v[14:15], v[2:3], 0, s[20:21]
	v_mov_b32_e32 v13, v115
	v_lshl_add_u64 v[14:15], v[14:15], 0, s[92:93]
	v_lshlrev_b64 v[12:13], 7, v[12:13]
	v_lshl_add_u64 v[14:15], v[14:15], 0, s[4:5]
	v_lshl_add_u64 v[12:13], s[10:11], 0, v[12:13]
	v_lshl_add_u64 v[14:15], v[14:15], 0, v[0:1]
	s_mov_b64 s[20:21], 0x100
	v_lshl_add_u64 v[12:13], v[12:13], 0, v[0:1]
	v_lshl_add_u64 v[16:17], v[14:15], 0, s[20:21]
	s_add_i32 m0, s14, 0x4000
	s_add_i32 s20, s0, 64
	global_load_lds_dwordx4 v[12:13], off
	v_or_b32_e32 v12, s20, v11
	v_mov_b32_e32 v13, v115
	v_lshlrev_b64 v[12:13], 7, v[12:13]
	s_add_i32 m0, s22, 0x6000
	v_lshl_add_u64 v[12:13], s[10:11], 0, v[12:13]
	global_load_lds_dwordx4 v[16:17], off
	v_lshl_add_u64 v[12:13], v[12:13], 0, v[0:1]
	s_mov_b64 s[20:21], 0x80
	s_add_i32 m0, s14, 0x8000
	v_lshl_add_u64 v[14:15], v[14:15], 0, s[20:21]
	s_add_i32 m0, s22, 0xa000
	v_mov_b32_e32 v5, s86
	ds_read_b128 v[12:15], v5
	v_mov_b32_e32 v5, s30
	ds_read_b128 v[16:19], v5
	s_waitcnt lgkmcnt(0)
	v_add_f32_e32 v5, v12, v13
	v_add_f32_e32 v5, v5, v14
	v_add_f32_e32 v5, v5, v15
	v_add_f32_e32 v5, v5, v16
	v_add_f32_e32 v5, v5, v17
	v_add_f32_e32 v5, v5, v18
	v_add_f32_e32 v5, v5, v19
	v_cvt_i32_f32_e32 v5, v5
	v_ashrrev_i32_e32 v5, 6, v5
	v_min_i32_e32 v5, s95, v5
	s_nop 0
	v_readfirstlane_b32 s33, v5
	s_cmp_lt_i32 s1, s33
	s_cbranch_scc1 .LBB0_570
	v_readlane_b32 s1, v236, 7
	s_add_i32 s14, s95, s1
	v_lshl_add_u64 v[2:3], v[2:3], 0, s[92:93]
	s_lshl_b32 s1, s14, 6
	v_lshl_add_u64 v[2:3], v[2:3], 0, s[4:5]
	s_or_b32 s5, s1, 32
	v_lshl_add_u64 v[128:129], v[2:3], 0, v[0:1]
	v_add_u32_e32 v2, s5, v4
	v_or_b32_e32 v3, 2, v2
	s_mov_b32 s6, s24
	v_cmp_gt_i32_e64 s[24:25], v3, v114
	v_or_b32_e32 v3, 3, v2
	v_cmp_gt_i32_e64 s[26:27], v3, v114
	v_or_b32_e32 v3, 4, v2
	v_cmp_gt_i32_e64 s[28:29], v3, v114
	v_or_b32_e32 v3, 5, v2
	s_mov_b32 s97, s31
	s_mov_b32 s96, s30
	v_cmp_gt_i32_e64 s[30:31], v3, v114
	v_or_b32_e32 v3, 6, v2
	s_mov_b64 s[8:9], s[34:35]
	v_cmp_gt_i32_e64 s[34:35], v3, v114
	v_or_b32_e32 v3, 7, v2
	v_cmp_gt_i32_e64 s[36:37], v3, v114
	v_add_u32_e32 v3, 16, v2
	v_cmp_gt_i32_e64 s[38:39], v3, v114
	v_add_u32_e32 v3, 17, v2
	v_cmp_gt_i32_e64 s[40:41], v3, v114
	v_add_u32_e32 v3, 18, v2
	v_cmp_gt_i32_e64 s[42:43], v3, v114
	v_add_u32_e32 v3, 19, v2
	v_lshl_add_u64 v[126:127], s[10:11], 0, v[0:1]
	v_and_b32_e32 v0, 0xffffffe0, v6
	v_cmp_gt_i32_e64 s[44:45], v3, v114
	v_add_u32_e32 v3, 20, v2
	v_add_u32_e32 v1, s13, v0
	v_cmp_gt_i32_e64 s[46:47], v3, v114
	v_add_u32_e32 v3, 21, v2
	v_lshl_add_u32 v150, s5, 2, v1
	v_cmp_gt_i32_e64 s[20:21], v2, v114
	v_cmp_lt_i32_e64 s[22:23], v2, v114
	v_cmp_gt_i32_e64 s[48:49], v3, v114
	v_add_u32_e32 v3, 22, v2
	v_add_u32_e32 v2, 23, v2
	v_lshl_add_u32 v152, s14, 8, v1
	v_add_u32_e32 v1, s1, v4
	v_cmp_gt_i32_e64 s[52:53], v2, v114
	v_or_b32_e32 v2, 2, v1
	v_cmp_gt_i32_e64 s[58:59], v2, v114
	v_or_b32_e32 v2, 3, v1
	v_cmp_gt_i32_e64 s[60:61], v2, v114
	v_or_b32_e32 v2, 4, v1
	v_cmp_gt_i32_e64 s[62:63], v2, v114
	v_or_b32_e32 v2, 5, v1
	v_cmp_gt_i32_e64 s[64:65], v2, v114
	v_or_b32_e32 v2, 6, v1
	v_cmp_gt_i32_e64 s[66:67], v2, v114
	v_or_b32_e32 v2, 7, v1
	v_cmp_gt_i32_e64 s[68:69], v2, v114
	v_add_u32_e32 v2, 16, v1
	v_cmp_gt_i32_e64 s[70:71], v2, v114
	v_add_u32_e32 v2, 17, v1
	v_cmp_gt_i32_e64 s[72:73], v2, v114
	v_add_u32_e32 v2, 18, v1
	v_cmp_gt_i32_e64 s[74:75], v2, v114
	v_add_u32_e32 v2, 19, v1
	v_cmp_gt_i32_e64 s[76:77], v2, v114
	v_add_u32_e32 v2, 20, v1
	s_add_i32 s1, s15, 0
	v_cmp_gt_i32_e64 s[78:79], v2, v114
	v_add_u32_e32 v2, 21, v1
	s_add_i32 s1, s1, 0x10300
	v_cmp_gt_i32_e64 s[54:55], v1, v114
	v_cmp_lt_i32_e64 s[56:57], v1, v114
	v_cmp_gt_i32_e64 s[80:81], v2, v114
	v_add_u32_e32 v2, 22, v1
	v_add_u32_e32 v1, 23, v1
	v_add_u32_e32 v153, s1, v0
	v_add_u32_e32 v0, s0, v8
	v_mov_b32_e32 v14, v115
	v_mov_b32_e32 v15, v115
	v_lshl_add_u32 v149, v6, 4, 0
	v_cmp_gt_i32_e64 s[50:51], v3, v114
	v_cmp_gt_i32_e64 s[82:83], v2, v114
	v_cmp_gt_i32_e64 s[84:85], v1, v114
	v_add3_u32 v130, v0, v10, v9
	s_sub_i32 s5, s95, s33
	v_mov_b32_e32 v0, v115
	v_mov_b32_e32 v1, v115
	v_mov_b32_e32 v2, v115
	v_mov_b32_e32 v3, v115
	v_mov_b32_e32 v4, v115
	v_mov_b32_e32 v5, v115
	v_mov_b32_e32 v6, v115
	v_mov_b32_e32 v7, v115
	v_mov_b32_e32 v8, v115
	v_mov_b32_e32 v9, v115
	v_mov_b32_e32 v10, v115
	v_mov_b32_e32 v11, v115
	v_mov_b32_e32 v12, v115
	v_mov_b32_e32 v13, v115
	v_mov_b64_e32 v[30:31], v[14:15]
	s_add_i32 s92, s5, 2
	s_mov_b32 s91, 0
	v_mov_b32_e32 v154, 0xff800000
	v_mov_b32_e32 v151, 0
	s_mov_b32 s15, 0
	v_mov_b64_e32 v[28:29], v[12:13]
	v_mov_b64_e32 v[26:27], v[10:11]
	v_mov_b64_e32 v[24:25], v[8:9]
	v_mov_b64_e32 v[22:23], v[6:7]
	v_mov_b64_e32 v[20:21], v[4:5]
	v_mov_b64_e32 v[18:19], v[2:3]
	v_mov_b64_e32 v[16:17], v[0:1]
	s_branch .LBB0_543

; template <int MODE>
; __device__ __forceinline__ void attn_fox_sub(const bf16x8 (&qr)[4], f32x16& O0, f32x16& O1, float& m, float& l, unsigned saddr  , unsigned cfaddr  , int j, int kv0, int q, int hi) {
;     bf16x8 kf[4], vf[2][2]; f32x4 c0, c1, c2, c3;
;     asm volatile("ds_read_b128 %0, %12\n\tds_read_b128 %1, %12 offset:1024\n\tds_read_b128 %2, %12 offset:2048\n\tds_read_b128 %3, %12 offset:3072\n\t"
;                  "ds_read_b128 %4, %13\n\tds_read_b128 %5, %13 offset:1024\n\tds_read_b128 %6, %13 offset:2048\n\tds_read_b128 %7, %13 offset:3072\n\t"
;                  "ds_read_b128 %8, %14\n\tds_read_b128 %9, %14 offset:16\n\tds_read_b128 %10, %14 offset:64\n\tds_read_b128 %11, %14 offset:80\n\ts_waitcnt lgkmcnt(0)"
;                  : "=&v"(kf[0]), "=&v"(kf[1]), "=&v"(kf[2]), "=&v"(kf[3]), "=&v"(vf[0][0]), "=&v"(vf[0][1]), "=&v"(vf[1][0]), "=&v"(vf[1][1]), "=&v"(c0), "=&v"(c1), "=&v"(c2), "=&v"(c3)
;                  : "v"(saddr + (unsigned)j * 4096u), "v"(saddr + 8192u + (unsigned)j * 4096u), "v"(cfaddr) : "memory");
;     f32x16 S;
; __device__ __forceinline__ void attn_fox_unit(Frame& F, const bf16_t* Qh, const bf16_t* Kh, const bf16_t* Vth, const float* CFh, const int qb, bf16_t* AOp, const float k2max) {
;     ...
;     for (int T = NT - 1; T >= Tmin; --T) {
;         if (T - Tmin >= 2) asm volatile("s_waitcnt vmcnt(4)" ::: "memory"); else if (T - Tmin == 1) asm volatile("s_waitcnt vmcnt(2)" ::: "memory"); else asm volatile("s_waitcnt vmcnt(0)" ::: "memory");
;         __builtin_amdgcn_s_barrier();
;         if (T - 3 >= Tmin) { const int fs = (slot + 3) & 3; attn_dma_tile(Kh, Vth, T - 3, ring + fs * AT_SLOT, wave, r32, r32p, hi); }
;         if (T <= my_last) {
;             const unsigned sa = ring_a + (unsigned)(slot * AT_SLOT);
;             if (T == my_last) {
;                 if (jdiag == 1) { attn_fox_sub<1>(qr, O0, O1, m, l, sa, cf_a + 4u * (unsigned)(64 * T + 32), 1, 64 * T + 32, q, hi); attn_fox_sub<0>(qr, O0, O1, m, l, sa, cf_a + 4u * (unsigned)(64 * T), 0, 64 * T, q, hi); }
;                 else attn_fox_sub<1>(qr, O0, O1, m, l, sa, cf_a + 4u * (unsigned)(64 * T), 0, 64 * T, q, hi);
;             } else { attn_fox_sub<0>(qr, O0, O1, m, l, sa, cf_a + 4u * (unsigned)(64 * T + 32), 1, 64 * T + 32, q, hi); attn_fox_sub<0>(qr, O0, O1, m, l, sa, cf_a + 4u * (unsigned)(64 * T), 0, 64 * T, q, hi); }
.LBB0_548:
	s_andn2_b64 vcc, exec, s[0:1]
	s_cbranch_vccnz .LBB0_550
	s_lshl_b32 s1, s15, 14
	s_add_i32 s1, s1, 0x8000
	s_and_b32 s1, s1, 0xc000
	v_add_u32_e32 v32, 64, v130
	v_ashrrev_i32_e32 v33, 31, v32
	v_lshlrev_b64 v[32:33], 7, v[32:33]
	v_lshl_add_u64 v[32:33], v[126:127], 0, v[32:33]
	s_ashr_i32 s13, s12, 31
	s_add_i32 m0, s1, s18
	s_add_i32 s0, s1, s19
	v_lshl_add_u64 v[34:35], s[12:13], 1, v[128:129]
	v_lshl_add_u64 v[34:35], v[34:35], 0, 64
	v_lshl_add_u64 v[34:35], v[34:35], 0, 64
	global_load_lds_dwordx4 v[32:33], off
	s_add_i32 m0, s0, 0x2000
	s_nop 0
	global_load_lds_dwordx4 v[34:35], off
	s_waitcnt vmcnt(4)
.LBB0_550:
	s_add_i32 s0, s95, s91
	s_cmp_lt_i32 s0, s33
	s_barrier
	s_cbranch_scc1 .LBB0_552
.LBB0_552:
	s_add_i32 s0, s0, 3
	s_cmp_gt_i32 s0, s14
	s_cbranch_scc1 .LBB0_542
	v_lshl_add_u32 v131, s15, 14, v149
	s_cmp_lg_u32 s16, s91
	s_mov_b64 s[0:1], -1
	s_cbranch_scc0 .LBB0_559
	v_add_u32_e32 v48, 0x80, v153
	v_add_u32_e32 v49, 0x1000, v131
	v_add_u32_e32 v50, 0x3000, v131
	ds_read_b128 v[32:35], v49
	ds_read_b128 v[36:39], v49 offset:1024
	ds_read_b128 v[40:43], v49 offset:2048
	ds_read_b128 v[44:47], v49 offset:3072
	ds_read_b128 v[64:67], v48
	ds_read_b128 v[68:71], v48 offset:16
	ds_read_b128 v[72:75], v48 offset:64
	ds_read_b128 v[76:79], v48 offset:80
	ds_read_b128 v[108:111], v50
	ds_read_b128 v[100:103], v50 offset:1024
	ds_read_b128 v[104:107], v50 offset:2048
	ds_read_b128 v[96:99], v50 offset:3072
	s_waitcnt lgkmcnt(4)
	v_mov_b32_e32 v155, v154
	v_mfma_f32_32x32x16_bf16 v[64:79], v[32:35], v[80:83], v[64:79]
	v_mov_b32_e32 v156, v151
	v_mfma_f32_32x32x16_bf16 v[64:79], v[36:39], v[84:87], v[64:79]
	v_mfma_f32_32x32x16_bf16 v[64:79], v[40:43], v[88:91], v[64:79]
	v_mfma_f32_32x32x16_bf16 v[64:79], v[44:47], v[92:95], v[64:79]
	s_nop 11
	v_max3_f32 v50, v64, v65, v66
	v_max3_f32 v48, v67, v68, v69
	v_max3_f32 v49, v70, v71, v72
	v_max3_f32 v50, v50, v48, v49
	v_max3_f32 v48, v73, v74, v75
	v_max3_f32 v49, v76, v77, v78
	v_max3_f32 v48, v48, v49, v79
	v_max_f32 v50, v50, v48
	v_mov_b32_e32 v48, v50
	s_nop 1
	v_permlane32_swap_b32_e32 v50, v48
	v_max_f32 v157, v50, v48
	v_cmp_gt_f32_e32 vcc, v157, v154
	s_cbranch_vccz .LBB0_556
	v_max3_f32 v155, v154, v157, s94
	v_sub_f32_e32 v32, v154, v155
	v_exp_f32_e32 v32, v32
	s_nop 0
	v_mul_f32_e32 v156, v151, v32
	v_pk_mul_f32 v[14:15], v[14:15], v[32:33] op_sel_hi:[1,0]
	v_pk_mul_f32 v[12:13], v[12:13], v[32:33] op_sel_hi:[1,0]
	v_pk_mul_f32 v[10:11], v[10:11], v[32:33] op_sel_hi:[1,0]
	v_pk_mul_f32 v[8:9], v[8:9], v[32:33] op_sel_hi:[1,0]
	v_pk_mul_f32 v[6:7], v[6:7], v[32:33] op_sel_hi:[1,0]
	v_pk_mul_f32 v[4:5], v[4:5], v[32:33] op_sel_hi:[1,0]
	v_pk_mul_f32 v[2:3], v[2:3], v[32:33] op_sel_hi:[1,0]
	v_pk_mul_f32 v[0:1], v[0:1], v[32:33] op_sel_hi:[1,0]
	v_pk_mul_f32 v[30:31], v[30:31], v[32:33] op_sel_hi:[1,0]
	v_pk_mul_f32 v[28:29], v[28:29], v[32:33] op_sel_hi:[1,0]
	v_pk_mul_f32 v[26:27], v[26:27], v[32:33] op_sel_hi:[1,0]
	v_pk_mul_f32 v[24:25], v[24:25], v[32:33] op_sel_hi:[1,0]
	v_pk_mul_f32 v[22:23], v[22:23], v[32:33] op_sel_hi:[1,0]
	v_pk_mul_f32 v[20:21], v[20:21], v[32:33] op_sel_hi:[1,0]
	v_pk_mul_f32 v[18:19], v[18:19], v[32:33] op_sel_hi:[1,0]
	v_pk_mul_f32 v[16:17], v[16:17], v[32:33] op_sel_hi:[1,0]

; __device__ __forceinline__ void attn_moba_unit(Frame& F, const bf16_t* Qh, const bf16_t* Kh, const bf16_t* Vth, const float* KMh, const float slope2, const int qb, bf16_t* AOp) {
;     ...
;     unsigned wsel = 0u;
; #pragma unroll
;     for (int n = 0; n < 8; ++n) if (__any((sel >> n) & 1u)) wsel |= 1u << n;
;     asm volatile("s_waitcnt vmcnt(0) lgkmcnt(0)" ::: "memory"); __builtin_amdgcn_s_barrier();
;     const int NT = 4 * qb + 4, my_last = 4 * qb + (wave >> 1), jdiag = wave & 1;
;     attn_dma_tile(Kh, Vth, NT - 1, ring, wave, r32, r32p, hi);
;     attn_dma_tile(Kh, Vth, NT - 2, ring + AT_SLOT, wave, r32, r32p, hi);
;     attn_dma_tile(Kh, Vth, NT - 3, ring + 2 * AT_SLOT, wave, r32, r32p, hi);
.LBB0_1298:
	v_lshlrev_b32_e32 v0, 1, v24
	v_and_b32_e32 v54, 8, v0
	v_and_b32_e32 v0, 1, v193
	v_lshrrev_b32_e32 v1, 1, v25
	v_cmp_ne_u32_e32 vcc, 0, v0
	v_and_b32_e32 v53, 4, v1
	s_cmp_lg_u64 vcc, 0
	v_bfe_u32 v1, v193, 1, 1
	s_cselect_b64 s[0:1], -1, 0
	v_cmp_ne_u32_e32 vcc, 0, v1
	v_cndmask_b32_e64 v0, 0, 1, s[0:1]
	s_cmp_eq_u64 vcc, 0
	s_cselect_b32 s0, 0, 2
	v_readfirstlane_b32 s1, v0
	v_bfe_u32 v0, v193, 2, 1
	s_or_b32 s0, s0, s1
	v_cmp_ne_u32_e32 vcc, 0, v0
	s_cmp_eq_u64 vcc, 0
	s_cselect_b32 s1, 0, 4
	v_bfe_u32 v0, v193, 3, 1
	s_or_b32 s0, s0, s1
	v_cmp_ne_u32_e32 vcc, 0, v0
	s_cmp_eq_u64 vcc, 0
	s_cselect_b32 s1, 0, 8
	v_bfe_u32 v0, v193, 4, 1
	s_or_b32 s0, s0, s1
	v_cmp_ne_u32_e32 vcc, 0, v0
	s_cmp_eq_u64 vcc, 0
	s_cselect_b32 s1, 0, 16
	v_bfe_u32 v0, v193, 5, 1
	s_or_b32 s0, s0, s1
	v_cmp_ne_u32_e32 vcc, 0, v0
	s_cmp_eq_u64 vcc, 0
	s_cselect_b32 s1, 0, 32
	v_bfe_u32 v0, v193, 6, 1
	s_or_b32 s0, s0, s1
	v_cmp_ne_u32_e32 vcc, 0, v0
	s_cmp_eq_u64 vcc, 0
	s_cselect_b32 s1, 0, 64
	s_lshl_b32 s78, s10, 2
	s_or_b32 s92, s78, 3
	v_and_b32_e32 v52, 19, v25
	s_or_b32 s79, s0, s1
	s_lshl_b32 s0, s92, 6
	v_or3_b32 v8, v53, v52, v54
	s_add_i32 s0, s0, s95
	v_or_b32_e32 v0, s0, v8
	v_readlane_b32 s0, v237, 58
	v_mov_b32_e32 v3, v161
	v_mov_b32_e32 v1, v161
	v_lshl_or_b32 v2, v24, 12, s0
	v_readlane_b32 s0, v236, 37
	v_readlane_b32 s1, v236, 38
	s_lshl_b32 s80, s92, 7
	v_lshlrev_b64 v[0:1], 7, v[0:1]
	v_lshl_add_u64 v[2:3], s[0:1], 0, v[2:3]
	v_lshl_add_u64 v[4:5], v[2:3], 0, s[80:81]
	s_lshl_b32 s80, s95, 1
	v_lshl_add_u64 v[0:1], s[2:3], 0, v[0:1]
	v_lshlrev_b64 v[50:51], 1, v[48:49]
	v_lshl_add_u64 v[4:5], v[4:5], 0, s[80:81]
	s_mov_b32 s75, s81
	s_add_i32 s4, s33, 0
	s_add_i32 s93, s91, 0x80
	v_lshl_add_u64 v[0:1], v[0:1], 0, v[50:51]
	v_lshl_add_u64 v[4:5], v[4:5], 0, s[74:75]
	s_mov_b32 m0, s4
	s_add_i32 s5, s88, 0
	s_add_i32 s0, s93, s95
	s_waitcnt vmcnt(0) lgkmcnt(0)
	s_barrier
; template <int MODE>
; __device__ __forceinline__ void attn_moba_sub(const bf16x8 (&qr)[4], f32x16& O0, f32x16& O1, float& m, float& l, unsigned saddr, int j, int kv0, int q, int q0, int hi, float slope2, bool rowok) {
;     ...
;     f32x16 S; const float sbase = slope2 * (float)(kv0 + 8 * hi - q0);
; #pragma unroll
;     for (int r = 0; r < 16; ++r) S[r] = sbase + slope2 * (float)((r & 7) + 16 * (r >> 3));
; __device__ __forceinline__ void attn_moba_unit(Frame& F, const bf16_t* Qh, const bf16_t* Kh, const bf16_t* Vth, const float* KMh, const float slope2, const int qb, bf16_t* AOp) {
;     ...
;     const int NT = 4 * qb + 4, my_last = 4 * qb + (wave >> 1), jdiag = wave & 1;
;     attn_dma_tile(Kh, Vth, NT - 1, ring, wave, r32, r32p, hi);
;     attn_dma_tile(Kh, Vth, NT - 2, ring + AT_SLOT, wave, r32, r32p, hi);
;     attn_dma_tile(Kh, Vth, NT - 3, ring + 2 * AT_SLOT, wave, r32, r32p, hi);
;     f32x16 O0 = f32x16{}, O1 = f32x16{}; float m = -INFINITY, l = 0.f;
;     int slot = 0;
	v_lshl_add_u64 v[4:5], v[4:5], 0, v[50:51]
	global_load_lds_dwordx4 v[0:1], off
	s_add_i32 m0, s5, 0x2000
	v_or_b32_e32 v0, s0, v8
	s_lshl_b32 s0, s91, 1
	s_mov_b32 s1, s81
	global_load_lds_dwordx4 v[4:5], off
	v_lshl_add_u64 v[4:5], v[2:3], 0, s[0:1]
	v_mov_b32_e32 v1, v161
	v_lshl_add_u64 v[4:5], v[4:5], 0, s[80:81]
	v_lshlrev_b64 v[0:1], 7, v[0:1]
	v_lshl_add_u64 v[4:5], v[4:5], 0, s[74:75]
	v_lshl_add_u64 v[0:1], s[2:3], 0, v[0:1]
	v_lshl_add_u64 v[4:5], v[4:5], 0, v[50:51]
	s_mov_b64 s[0:1], 0x100
	s_add_i32 s70, s91, s95
	v_lshl_add_u64 v[0:1], v[0:1], 0, v[50:51]
	v_lshl_add_u64 v[6:7], v[4:5], 0, s[0:1]
	s_add_i32 m0, s4, 0x4000
	s_add_i32 s0, s70, 64
	global_load_lds_dwordx4 v[0:1], off
	v_or_b32_e32 v0, s0, v8
	v_mov_b32_e32 v1, v161
	v_lshlrev_b64 v[0:1], 7, v[0:1]
	s_add_i32 m0, s5, 0x6000
	v_lshl_add_u64 v[0:1], s[2:3], 0, v[0:1]
	global_load_lds_dwordx4 v[6:7], off
	v_lshl_add_u64 v[0:1], v[0:1], 0, v[50:51]
	s_mov_b64 s[0:1], 0x80
	s_add_i32 m0, s4, 0x8000
	v_lshl_add_u64 v[4:5], v[4:5], 0, s[0:1]
	s_add_i32 m0, s5, 0xa000
	s_add_i32 s87, s78, s73
	s_lshl_b32 s0, s87, 6
	v_add_u32_e32 v49, s0, v48
	v_add_u32_e32 v16, 32, v49
	v_lshl_add_u64 v[0:1], v[2:3], 0, s[80:81]
	v_subrev_u32_e32 v2, s38, v16
	v_cmp_gt_i32_e64 s[4:5], v16, v160
	v_cmp_lt_i32_e64 s[6:7], v16, v160
	v_add_u32_e32 v16, 34, v49
	v_cmp_gt_i32_e64 s[8:9], v16, v160
	v_add_u32_e32 v16, 35, v49
	v_cmp_gt_i32_e64 s[10:11], v16, v160
	v_add_u32_e32 v16, 36, v49
	v_cmp_gt_i32_e64 s[12:13], v16, v160
	v_add_u32_e32 v16, 37, v49
	v_cmp_gt_i32_e64 s[14:15], v16, v160
	v_add_u32_e32 v16, 38, v49
	v_or_b32_e32 v55, 2, v49
	v_cmp_gt_i32_e64 s[16:17], v16, v160
	v_add_u32_e32 v16, 39, v49
	v_cmp_gt_i32_e64 s[42:43], v55, v160
	v_or_b32_e32 v55, 3, v49
	v_cmp_gt_i32_e64 s[18:19], v16, v160
	v_add_u32_e32 v16, 48, v49
	v_cmp_gt_i32_e64 s[44:45], v55, v160
	v_or_b32_e32 v55, 4, v49
	v_cmp_gt_i32_e64 s[20:21], v16, v160
	v_add_u32_e32 v16, 49, v49
	v_cmp_gt_i32_e64 s[46:47], v55, v160
	v_or_b32_e32 v55, 5, v49
	v_subrev_u32_e32 v17, s38, v48
	v_cmp_gt_i32_e64 s[22:23], v16, v160
	v_add_u32_e32 v16, 50, v49
	v_cmp_gt_i32_e64 s[48:49], v55, v160
	v_or_b32_e32 v55, 6, v49
	v_cmp_gt_i32_e64 s[24:25], v16, v160
	v_add_u32_e32 v16, 51, v49
	v_add_u32_e32 v17, s0, v17
	v_cmp_gt_i32_e64 s[50:51], v55, v160
	v_or_b32_e32 v55, 7, v49
	v_cmp_gt_i32_e64 s[26:27], v16, v160
	v_add_u32_e32 v16, 52, v49
	v_cvt_f32_i32_e32 v17, v17
	v_cmp_gt_i32_e64 s[52:53], v55, v160
	v_add_u32_e32 v55, 16, v49
	v_cmp_gt_i32_e64 s[28:29], v16, v160
	v_add_u32_e32 v16, 53, v49
	v_cmp_gt_i32_e64 s[54:55], v55, v160
	v_add_u32_e32 v55, 17, v49
	v_cmp_gt_i32_e64 s[30:31], v16, v160
	v_add_u32_e32 v16, 54, v49
	v_cmp_gt_i32_e64 s[56:57], v55, v160
	v_add_u32_e32 v55, 18, v49
	v_cmp_gt_i32_e64 s[34:35], v16, v160
	v_add_u32_e32 v16, 55, v49
	v_cmp_gt_i32_e64 s[58:59], v55, v160
	v_add_u32_e32 v55, 19, v49
	v_cmp_gt_i32_e64 s[36:37], v16, v160
	v_mul_f32_e32 v16, v163, v17
	v_cmp_gt_i32_e64 s[60:61], v55, v160
	v_add_u32_e32 v55, 20, v49
	v_lshl_add_u32 v194, v25, 4, 0
	v_pk_add_f32 v[30:31], v[176:177], v[16:17] op_sel_hi:[1,0]
	v_pk_add_f32 v[28:29], v[174:175], v[16:17] op_sel_hi:[1,0]
	v_pk_add_f32 v[26:27], v[172:173], v[16:17] op_sel_hi:[1,0]
	v_pk_add_f32 v[24:25], v[170:171], v[16:17] op_sel_hi:[1,0]
	v_pk_add_f32 v[22:23], v[168:169], v[16:17] op_sel_hi:[1,0]
	v_subrev_u32_e32 v17, s38, v49
	v_cmp_gt_i32_e64 s[62:63], v55, v160
	v_add_u32_e32 v55, 21, v49
	v_readlane_b32 s0, v236, 34
	v_cvt_f32_i32_e32 v2, v2
	v_cvt_f32_i32_e32 v32, v17
	v_cmp_gt_i32_e64 s[38:39], v49, v160
	v_cmp_lt_i32_e64 s[40:41], v49, v160
	v_cmp_gt_i32_e64 s[64:65], v55, v160
	v_add_u32_e32 v55, 22, v49
	v_add_u32_e32 v49, 23, v49
	v_add_u32_e32 v195, s0, v48
	v_add_u32_e32 v48, s70, v52
	v_cmp_gt_i32_e64 s[68:69], v49, v160
	v_add3_u32 v48, v48, v54, v53
	v_mov_b32_e32 v49, v161
	v_lshlrev_b64 v[48:49], 7, v[48:49]
	v_lshl_add_u64 v[0:1], v[0:1], 0, s[74:75]
	v_lshl_add_u64 v[48:49], v[48:49], 0, v[50:51]
	v_mov_b32_e32 v62, v161
	v_mov_b32_e32 v63, v161
	v_lshl_add_u64 v[178:179], v[0:1], 0, v[50:51]
	v_mul_f32_e32 v0, v163, v2
	v_mul_f32_e32 v32, v163, v32
	v_cmp_gt_i32_e64 s[66:67], v55, v160
	v_lshl_add_u64 v[180:181], s[96:97], 0, v[48:49]
	v_mov_b32_e32 v48, v161
	v_mov_b32_e32 v49, v161
	v_mov_b32_e32 v50, v161
	v_mov_b32_e32 v51, v161
	v_mov_b32_e32 v52, v161
	v_mov_b32_e32 v53, v161
	v_mov_b32_e32 v54, v161
	v_mov_b32_e32 v55, v161
	v_mov_b32_e32 v56, v161
	v_mov_b32_e32 v57, v161
	v_mov_b32_e32 v58, v161
	v_mov_b32_e32 v59, v161
	v_mov_b32_e32 v60, v161
	v_mov_b32_e32 v61, v161
	v_mov_b64_e32 v[78:79], v[62:63]
	s_mov_b32 s89, 0
	v_pk_add_f32 v[14:15], v[176:177], v[0:1] op_sel_hi:[1,0]
	v_pk_add_f32 v[12:13], v[174:175], v[0:1] op_sel_hi:[1,0]
	v_pk_add_f32 v[10:11], v[172:173], v[0:1] op_sel_hi:[1,0]
	v_pk_add_f32 v[8:9], v[170:171], v[0:1] op_sel_hi:[1,0]
	v_pk_add_f32 v[6:7], v[168:169], v[0:1] op_sel_hi:[1,0]
	v_pk_add_f32 v[4:5], v[166:167], v[0:1] op_sel_hi:[1,0]
	v_pk_add_f32 v[2:3], v[164:165], v[0:1] op_sel_hi:[1,0]
	v_pk_add_f32 v[0:1], v[162:163], v[0:1] op_sel_hi:[1,0]
	v_pk_add_f32 v[20:21], v[166:167], v[16:17] op_sel_hi:[1,0]
	v_pk_add_f32 v[18:19], v[164:165], v[16:17] op_sel_hi:[1,0]
	v_pk_add_f32 v[16:17], v[162:163], v[16:17] op_sel_hi:[1,0]
	v_pk_add_f32 v[46:47], v[176:177], v[32:33] op_sel_hi:[1,0]
	v_pk_add_f32 v[44:45], v[174:175], v[32:33] op_sel_hi:[1,0]
	v_pk_add_f32 v[42:43], v[172:173], v[32:33] op_sel_hi:[1,0]
	v_pk_add_f32 v[40:41], v[170:171], v[32:33] op_sel_hi:[1,0]
	v_pk_add_f32 v[38:39], v[168:169], v[32:33] op_sel_hi:[1,0]
	v_pk_add_f32 v[36:37], v[166:167], v[32:33] op_sel_hi:[1,0]
	v_pk_add_f32 v[34:35], v[164:165], v[32:33] op_sel_hi:[1,0]
	v_pk_add_f32 v[32:33], v[162:163], v[32:33] op_sel_hi:[1,0]
	s_add_i32 s75, s91, 0x100
	v_mov_b32_e32 v196, 0xff800000
	v_mov_b32_e32 v197, 0
	s_mov_b32 s72, 0
	v_mov_b64_e32 v[76:77], v[60:61]
	v_mov_b64_e32 v[74:75], v[58:59]
	v_mov_b64_e32 v[72:73], v[56:57]
	v_mov_b64_e32 v[70:71], v[54:55]
	v_mov_b64_e32 v[68:69], v[52:53]
	v_mov_b64_e32 v[66:67], v[50:51]
	v_mov_b64_e32 v[64:65], v[48:49]
	s_cmp_lt_u32 s92, 2
	s_mov_b64 s[0:1], -1
	s_cbranch_scc0 .LBB0_1305
	s_branch .LBB0_1300

; __device__ __forceinline__ void attn_moba_unit(Frame& F, const bf16_t* Qh, const bf16_t* Kh, const bf16_t* Vth, const float* KMh, const float slope2, const int qb, bf16_t* AOp) {
;     ...
; #pragma unroll 1
;     for (int T = NT - 1; T >= 0; --T) {
;         if (T >= 2) asm volatile("s_waitcnt vmcnt(4)" ::: "memory"); else if (T == 1) asm volatile("s_waitcnt vmcnt(2)" ::: "memory"); else asm volatile("s_waitcnt vmcnt(0)" ::: "memory");
;         __builtin_amdgcn_s_barrier();
;         if (T >= 3) { const int fs = (slot + 3) & 3; attn_dma_tile(Kh, Vth, T - 3, ring + fs * AT_SLOT, wave, r32, r32p, hi); }
;         const unsigned sa = ring_a + (unsigned)(slot * AT_SLOT);
;         if (T >= 4 * qb) {
;             if (T == my_last) {
;                 if (jdiag == 1) { attn_moba_sub<1>(qr, O0, O1, m, l, sa, 1, 64 * T + 32, q, q0, hi, slope2, true); attn_moba_sub<0>(qr, O0, O1, m, l, sa, 0, 64 * T, q, q0, hi, slope2, true); }
;                 else attn_moba_sub<1>(qr, O0, O1, m, l, sa, 0, 64 * T, q, q0, hi, slope2, true);
;             } else if (T < my_last) { attn_moba_sub<0>(qr, O0, O1, m, l, sa, 1, 64 * T + 32, q, q0, hi, slope2, true); attn_moba_sub<0>(qr, O0, O1, m, l, sa, 0, 64 * T, q, q0, hi, slope2, true); }
.LBB0_1305:
	s_andn2_b64 vcc, exec, s[0:1]
	s_cbranch_vccnz .LBB0_1307
	s_lshl_b32 s0, s72, 14
	s_add_i32 s1, s0, 0x8000
	s_and_b32 s1, s1, 0xc000
	s_add_i32 s80, s91, s89
	s_add_i32 s80, s80, 64
	s_add_i32 m0, s1, s33
	s_add_i32 s70, s1, s88
	v_lshl_add_u64 v[80:81], s[80:81], 1, v[178:179]
	s_mov_b64 s[0:1], 0x2000
	v_lshl_add_u64 v[82:83], v[180:181], 0, s[0:1]
	global_load_lds_dwordx4 v[82:83], off
	s_add_i32 m0, s70, 0x2000
	s_nop 0
	global_load_lds_dwordx4 v[80:81], off
	s_waitcnt vmcnt(4)
.LBB0_1307:
	s_lshl_b32 s0, s72, 14
	s_cmp_lt_u32 s92, 3
	s_barrier
	s_cbranch_scc1 .LBB0_1309
.LBB0_1309:
	v_add_u32_e32 v198, s0, v194
	s_cmp_lt_i32 s92, s78
	s_mov_b64 s[0:1], -1
	s_cbranch_scc1 .LBB0_1330
	s_cmp_lg_u32 s90, s89
	s_cbranch_scc0 .LBB0_1318
	v_mov_b64_e32 v[110:111], v[62:63]
	v_mov_b64_e32 v[94:95], v[78:79]
	s_cmp_ge_i32 s92, s87
	v_mov_b64_e32 v[108:109], v[60:61]
	v_mov_b64_e32 v[106:107], v[58:59]
	v_mov_b64_e32 v[104:105], v[56:57]
	v_mov_b64_e32 v[102:103], v[54:55]
	v_mov_b64_e32 v[100:101], v[52:53]
	v_mov_b64_e32 v[98:99], v[50:51]
	v_mov_b64_e32 v[96:97], v[48:49]
	v_mov_b64_e32 v[92:93], v[76:77]
	v_mov_b64_e32 v[90:91], v[74:75]
	v_mov_b64_e32 v[88:89], v[72:73]
	v_mov_b64_e32 v[86:87], v[70:71]
	v_mov_b64_e32 v[84:85], v[68:69]
	v_mov_b64_e32 v[82:83], v[66:67]
	v_mov_b64_e32 v[80:81], v[64:65]
	v_mov_b32_e32 v116, v197
	v_mov_b32_e32 v199, v196
	s_cbranch_scc1 .LBB0_1317
	v_add_u32_e32 v201, s89, v195
	v_add_u32_e32 v80, 0xe0, v201
	v_cvt_f32_i32_e32 v96, v80
	v_add_u32_e32 v97, 0x1000, v198
	v_add_u32_e32 v98, 0x3000, v198
	ds_read_b128 v[80:83], v97
	ds_read_b128 v[84:87], v97 offset:1024
	ds_read_b128 v[88:91], v97 offset:2048
	ds_read_b128 v[92:95], v97 offset:3072
	ds_read_b128 v[156:159], v98
	ds_read_b128 v[148:151], v98 offset:1024
	ds_read_b128 v[152:155], v98 offset:2048
	ds_read_b128 v[144:147], v98 offset:3072
	s_waitcnt lgkmcnt(4)
	v_mul_f32_e32 v96, v163, v96
	v_pk_add_f32 v[126:127], v[176:177], v[96:97] op_sel_hi:[1,0]
	v_pk_add_f32 v[124:125], v[174:175], v[96:97] op_sel_hi:[1,0]
	v_pk_add_f32 v[122:123], v[172:173], v[96:97] op_sel_hi:[1,0]
	v_pk_add_f32 v[120:121], v[170:171], v[96:97] op_sel_hi:[1,0]
	v_pk_add_f32 v[118:119], v[168:169], v[96:97] op_sel_hi:[1,0]
	v_pk_add_f32 v[116:117], v[166:167], v[96:97] op_sel_hi:[1,0]
	v_pk_add_f32 v[114:115], v[164:165], v[96:97] op_sel_hi:[1,0]
	v_pk_add_f32 v[112:113], v[162:163], v[96:97] op_sel_hi:[1,0]
	v_mov_b32_e32 v199, v196
	v_mov_b32_e32 v200, v197
	v_mfma_f32_32x32x16_bf16 v[112:127], v[80:83], v[128:131], v[112:127]
	v_mfma_f32_32x32x16_bf16 v[112:127], v[84:87], v[132:135], v[112:127]
	v_mfma_f32_32x32x16_bf16 v[112:127], v[88:91], v[136:139], v[112:127]
	v_mfma_f32_32x32x16_bf16 v[112:127], v[92:95], v[140:143], v[112:127]
	s_nop 11
	v_max3_f32 v98, v112, v113, v114
	v_max3_f32 v96, v115, v116, v117
	v_max3_f32 v97, v118, v119, v120
	v_max3_f32 v98, v98, v96, v97
	v_max3_f32 v96, v121, v122, v123
	v_max3_f32 v97, v124, v125, v126
	v_max3_f32 v96, v96, v97, v127
	v_max_f32 v98, v98, v96
	v_mov_b64_e32 v[94:95], v[78:79]
	v_mov_b32_e32 v96, v98
	s_nop 1
	v_permlane32_swap_b32_e32 v98, v96
	v_max_f32 v202, v98, v96
	v_mov_b64_e32 v[110:111], v[62:63]
	v_mov_b64_e32 v[92:93], v[76:77]
	v_mov_b64_e32 v[90:91], v[74:75]
	v_mov_b64_e32 v[88:89], v[72:73]
	v_mov_b64_e32 v[86:87], v[70:71]
	v_mov_b64_e32 v[84:85], v[68:69]
	v_mov_b64_e32 v[82:83], v[66:67]
	v_mov_b64_e32 v[80:81], v[64:65]
	v_cmp_gt_f32_e32 vcc, v202, v196
	v_mov_b64_e32 v[108:109], v[60:61]
	v_mov_b64_e32 v[106:107], v[58:59]
	v_mov_b64_e32 v[104:105], v[56:57]
	v_mov_b64_e32 v[102:103], v[54:55]
	v_mov_b64_e32 v[100:101], v[52:53]
	v_mov_b64_e32 v[98:99], v[50:51]
	v_mov_b64_e32 v[96:97], v[48:49]
	s_cbranch_vccz .LBB0_1314
	v_max3_f32 v199, v196, v202, s86
	v_sub_f32_e32 v80, v196, v199
	v_exp_f32_e32 v80, v80
	s_nop 0
	v_mul_f32_e32 v200, v197, v80
	v_pk_mul_f32 v[110:111], v[62:63], v[80:81] op_sel_hi:[1,0]
	v_pk_mul_f32 v[108:109], v[60:61], v[80:81] op_sel_hi:[1,0]
	v_pk_mul_f32 v[106:107], v[58:59], v[80:81] op_sel_hi:[1,0]
	v_pk_mul_f32 v[104:105], v[56:57], v[80:81] op_sel_hi:[1,0]
	v_pk_mul_f32 v[102:103], v[54:55], v[80:81] op_sel_hi:[1,0]
	v_pk_mul_f32 v[100:101], v[52:53], v[80:81] op_sel_hi:[1,0]
	v_pk_mul_f32 v[98:99], v[50:51], v[80:81] op_sel_hi:[1,0]
	v_pk_mul_f32 v[96:97], v[48:49], v[80:81] op_sel_hi:[1,0]
	v_pk_mul_f32 v[94:95], v[78:79], v[80:81] op_sel_hi:[1,0]
	v_pk_mul_f32 v[92:93], v[76:77], v[80:81] op_sel_hi:[1,0]
	v_pk_mul_f32 v[90:91], v[74:75], v[80:81] op_sel_hi:[1,0]
	v_pk_mul_f32 v[88:89], v[72:73], v[80:81] op_sel_hi:[1,0]
	v_pk_mul_f32 v[86:87], v[70:71], v[80:81] op_sel_hi:[1,0]
	v_pk_mul_f32 v[84:85], v[68:69], v[80:81] op_sel_hi:[1,0]
	v_pk_mul_f32 v[82:83], v[66:67], v[80:81] op_sel_hi:[1,0]
	v_pk_mul_f32 v[80:81], v[64:65], v[80:81] op_sel_hi:[1,0]
